# layers 1-3: 5 rotating edge slots (10 row loads in flight per group) at 7 blocks per CU with 72 VGPRs
# baseline (speedup 1.0000x reference)
.LBB5_24:
	v_or_b32_e32 v46, 1, v35
	v_add_u32_e32 v46, s24, v46
	v_min_i32_e32 v46, 0x1869f, v46
	v_lshl_add_u32 v46, v46, 8, v26
	global_load_dwordx4 v[30:33], v46, s[4:5]
	s_mov_b64 s[22:23], exec
	s_movk_i32 s0, 0x2200
	v_sub_u32_e32 v27, v44, v28
	v_lshl_add_u32 v27, v27, 2, s0
	v_lshl_add_u32 v29, v44, 8, v26
	v_cmp_lt_i32_e64 s[2:3], v44, v45
	v_add_u32_e32 v46, 1, v44
	v_cmp_lt_i32_e64 s[16:17], v46, v45
	v_add_u32_e32 v46, 2, v44
	v_cmp_lt_i32_e64 s[18:19], v46, v45
	v_add_u32_e32 v46, 3, v44
	v_cmp_lt_i32_e64 s[20:21], v46, v45
	v_add_u32_e32 v46, 4, v44
	v_cmp_lt_i32_e64 s[14:15], v46, v45
	s_mov_b64 exec, s[2:3]
	ds_read_b32 v2, v27 offset:0
	global_load_dwordx4 v[4:7], v29, s[12:13] offset:0
	s_waitcnt lgkmcnt(0)
	v_lshl_add_u32 v2, v2, 8, v26
	global_load_dwordx4 v[8:11], v2, s[4:5]
	ds_read_b32 v2, v27 offset:20
	s_mov_b64 exec, s[16:17]
	ds_read_b32 v3, v27 offset:4
	global_load_dwordx4 v[12:15], v29, s[12:13] offset:256
	s_waitcnt lgkmcnt(0)
	v_lshl_add_u32 v3, v3, 8, v26
	global_load_dwordx4 v[16:19], v3, s[4:5]
	ds_read_b32 v3, v27 offset:24
	s_mov_b64 exec, s[18:19]
	ds_read_b32 v24, v27 offset:8
	global_load_dwordx4 v[20:23], v29, s[12:13] offset:512
	s_waitcnt lgkmcnt(0)
	v_lshl_add_u32 v24, v24, 8, v26
	global_load_dwordx4 v[50:53], v24, s[4:5]
	ds_read_b32 v24, v27 offset:28
	s_mov_b64 exec, s[20:21]
	ds_read_b32 v25, v27 offset:12
	global_load_dwordx4 v[54:57], v29, s[12:13] offset:768
	s_waitcnt lgkmcnt(0)
	v_lshl_add_u32 v25, v25, 8, v26
	global_load_dwordx4 v[58:61], v25, s[4:5]
	ds_read_b32 v25, v27 offset:32
	s_mov_b64 exec, s[14:15]
	ds_read_b32 v62, v27 offset:16
	global_load_dwordx4 v[64:67], v29, s[12:13] offset:1024
	s_waitcnt lgkmcnt(0)
	v_lshl_add_u32 v62, v62, 8, v26
	global_load_dwordx4 v[68:71], v62, s[4:5]
	ds_read_b32 v62, v27 offset:36
	s_mov_b64 exec, s[22:23]
	s_cmp_eq_u64 s[2:3], 0
	s_cbranch_scc1 .Ll5_p1_empty
.Ll5_p1_loop:
	s_mov_b64 exec, s[2:3]
	s_waitcnt vmcnt(8)
	v_fma_mix_f32 v46, v8, 1.0, v4 op_sel_hi:[1,0,1]
	v_fma_mix_f32 v47, v8, 1.0, v4 op_sel:[1,0,1] op_sel_hi:[1,0,1]
	v_fma_mix_f32 v48, v9, 1.0, v5 op_sel_hi:[1,0,1]
	v_fma_mix_f32 v49, v9, 1.0, v5 op_sel:[1,0,1] op_sel_hi:[1,0,1]
	v_max_f32_e32 v46, 0, v46
	v_max_f32_e32 v47, 0, v47
	v_max_f32_e32 v48, 0, v48
	v_max_f32_e32 v49, 0, v49
	v_pk_add_f32 v[42:43], v[42:43], v[46:47]
	v_pk_add_f32 v[40:41], v[40:41], v[48:49]
	v_fma_mix_f32 v46, v10, 1.0, v6 op_sel_hi:[1,0,1]
	v_fma_mix_f32 v47, v10, 1.0, v6 op_sel:[1,0,1] op_sel_hi:[1,0,1]
	v_fma_mix_f32 v48, v11, 1.0, v7 op_sel_hi:[1,0,1]
	v_fma_mix_f32 v49, v11, 1.0, v7 op_sel:[1,0,1] op_sel_hi:[1,0,1]
	v_max_f32_e32 v46, 0, v46
	v_max_f32_e32 v47, 0, v47
	v_max_f32_e32 v48, 0, v48
	v_max_f32_e32 v49, 0, v49
	v_pk_add_f32 v[38:39], v[38:39], v[46:47]
	v_pk_add_f32 v[36:37], v[36:37], v[48:49]
	v_add_u32_e32 v46, 5, v44
	v_cmp_lt_i32_e64 s[2:3], v46, v45
	s_mov_b64 exec, s[2:3]
	global_load_dwordx4 v[4:7], v29, s[12:13] offset:1280
	s_waitcnt lgkmcnt(0)
	v_lshl_add_u32 v2, v2, 8, v26
	global_load_dwordx4 v[8:11], v2, s[4:5]
	ds_read_b32 v2, v27 offset:40
	s_mov_b64 exec, s[16:17]
	s_waitcnt vmcnt(8)
	v_fma_mix_f32 v46, v16, 1.0, v12 op_sel_hi:[1,0,1]
	v_fma_mix_f32 v47, v16, 1.0, v12 op_sel:[1,0,1] op_sel_hi:[1,0,1]
	v_fma_mix_f32 v48, v17, 1.0, v13 op_sel_hi:[1,0,1]
	v_fma_mix_f32 v49, v17, 1.0, v13 op_sel:[1,0,1] op_sel_hi:[1,0,1]
	v_max_f32_e32 v46, 0, v46
	v_max_f32_e32 v47, 0, v47
	v_max_f32_e32 v48, 0, v48
	v_max_f32_e32 v49, 0, v49
	v_pk_add_f32 v[42:43], v[42:43], v[46:47]
	v_pk_add_f32 v[40:41], v[40:41], v[48:49]
	v_fma_mix_f32 v46, v18, 1.0, v14 op_sel_hi:[1,0,1]
	v_fma_mix_f32 v47, v18, 1.0, v14 op_sel:[1,0,1] op_sel_hi:[1,0,1]
	v_fma_mix_f32 v48, v19, 1.0, v15 op_sel_hi:[1,0,1]
	v_fma_mix_f32 v49, v19, 1.0, v15 op_sel:[1,0,1] op_sel_hi:[1,0,1]
	v_max_f32_e32 v46, 0, v46
	v_max_f32_e32 v47, 0, v47
	v_max_f32_e32 v48, 0, v48
	v_max_f32_e32 v49, 0, v49
	v_pk_add_f32 v[38:39], v[38:39], v[46:47]
	v_pk_add_f32 v[36:37], v[36:37], v[48:49]
	v_add_u32_e32 v46, 6, v44
	v_cmp_lt_i32_e64 s[16:17], v46, v45
	s_mov_b64 exec, s[16:17]
	global_load_dwordx4 v[12:15], v29, s[12:13] offset:1536
	s_waitcnt lgkmcnt(0)
	v_lshl_add_u32 v3, v3, 8, v26
	global_load_dwordx4 v[16:19], v3, s[4:5]
	ds_read_b32 v3, v27 offset:44
	s_mov_b64 exec, s[18:19]
	s_waitcnt vmcnt(8)
	v_fma_mix_f32 v46, v50, 1.0, v20 op_sel_hi:[1,0,1]
	v_fma_mix_f32 v47, v50, 1.0, v20 op_sel:[1,0,1] op_sel_hi:[1,0,1]
	v_fma_mix_f32 v48, v51, 1.0, v21 op_sel_hi:[1,0,1]
	v_fma_mix_f32 v49, v51, 1.0, v21 op_sel:[1,0,1] op_sel_hi:[1,0,1]
	v_max_f32_e32 v46, 0, v46
	v_max_f32_e32 v47, 0, v47
	v_max_f32_e32 v48, 0, v48
	v_max_f32_e32 v49, 0, v49
	v_pk_add_f32 v[42:43], v[42:43], v[46:47]
	v_pk_add_f32 v[40:41], v[40:41], v[48:49]
	v_fma_mix_f32 v46, v52, 1.0, v22 op_sel_hi:[1,0,1]
	v_fma_mix_f32 v47, v52, 1.0, v22 op_sel:[1,0,1] op_sel_hi:[1,0,1]
	v_fma_mix_f32 v48, v53, 1.0, v23 op_sel_hi:[1,0,1]
	v_fma_mix_f32 v49, v53, 1.0, v23 op_sel:[1,0,1] op_sel_hi:[1,0,1]
	v_max_f32_e32 v46, 0, v46
	v_max_f32_e32 v47, 0, v47
	v_max_f32_e32 v48, 0, v48
	v_max_f32_e32 v49, 0, v49
	v_pk_add_f32 v[38:39], v[38:39], v[46:47]
	v_pk_add_f32 v[36:37], v[36:37], v[48:49]
	v_add_u32_e32 v46, 7, v44
	v_cmp_lt_i32_e64 s[18:19], v46, v45
	s_mov_b64 exec, s[18:19]
	global_load_dwordx4 v[20:23], v29, s[12:13] offset:1792
	s_waitcnt lgkmcnt(0)
	v_lshl_add_u32 v24, v24, 8, v26
	global_load_dwordx4 v[50:53], v24, s[4:5]
	ds_read_b32 v24, v27 offset:48
	s_mov_b64 exec, s[20:21]
	s_waitcnt vmcnt(8)
	v_fma_mix_f32 v46, v58, 1.0, v54 op_sel_hi:[1,0,1]
	v_fma_mix_f32 v47, v58, 1.0, v54 op_sel:[1,0,1] op_sel_hi:[1,0,1]
	v_fma_mix_f32 v48, v59, 1.0, v55 op_sel_hi:[1,0,1]
	v_fma_mix_f32 v49, v59, 1.0, v55 op_sel:[1,0,1] op_sel_hi:[1,0,1]
	v_max_f32_e32 v46, 0, v46
	v_max_f32_e32 v47, 0, v47
	v_max_f32_e32 v48, 0, v48
	v_max_f32_e32 v49, 0, v49
	v_pk_add_f32 v[42:43], v[42:43], v[46:47]
	v_pk_add_f32 v[40:41], v[40:41], v[48:49]
	v_fma_mix_f32 v46, v60, 1.0, v56 op_sel_hi:[1,0,1]
	v_fma_mix_f32 v47, v60, 1.0, v56 op_sel:[1,0,1] op_sel_hi:[1,0,1]
	v_fma_mix_f32 v48, v61, 1.0, v57 op_sel_hi:[1,0,1]
	v_fma_mix_f32 v49, v61, 1.0, v57 op_sel:[1,0,1] op_sel_hi:[1,0,1]
	v_max_f32_e32 v46, 0, v46
	v_max_f32_e32 v47, 0, v47
	v_max_f32_e32 v48, 0, v48
	v_max_f32_e32 v49, 0, v49
	v_pk_add_f32 v[38:39], v[38:39], v[46:47]
	v_pk_add_f32 v[36:37], v[36:37], v[48:49]
	v_add_u32_e32 v46, 8, v44
	v_cmp_lt_i32_e64 s[20:21], v46, v45
	s_mov_b64 exec, s[20:21]
	global_load_dwordx4 v[54:57], v29, s[12:13] offset:2048
	s_waitcnt lgkmcnt(0)
	v_lshl_add_u32 v25, v25, 8, v26
	global_load_dwordx4 v[58:61], v25, s[4:5]
	ds_read_b32 v25, v27 offset:52
	s_mov_b64 exec, s[14:15]
	s_waitcnt vmcnt(8)
	v_fma_mix_f32 v46, v68, 1.0, v64 op_sel_hi:[1,0,1]
	v_fma_mix_f32 v47, v68, 1.0, v64 op_sel:[1,0,1] op_sel_hi:[1,0,1]
	v_fma_mix_f32 v48, v69, 1.0, v65 op_sel_hi:[1,0,1]
	v_fma_mix_f32 v49, v69, 1.0, v65 op_sel:[1,0,1] op_sel_hi:[1,0,1]
	v_max_f32_e32 v46, 0, v46
	v_max_f32_e32 v47, 0, v47
	v_max_f32_e32 v48, 0, v48
	v_max_f32_e32 v49, 0, v49
	v_pk_add_f32 v[42:43], v[42:43], v[46:47]
	v_pk_add_f32 v[40:41], v[40:41], v[48:49]
	v_fma_mix_f32 v46, v70, 1.0, v66 op_sel_hi:[1,0,1]
	v_fma_mix_f32 v47, v70, 1.0, v66 op_sel:[1,0,1] op_sel_hi:[1,0,1]
	v_fma_mix_f32 v48, v71, 1.0, v67 op_sel_hi:[1,0,1]
	v_fma_mix_f32 v49, v71, 1.0, v67 op_sel:[1,0,1] op_sel_hi:[1,0,1]
	v_max_f32_e32 v46, 0, v46
	v_max_f32_e32 v47, 0, v47
	v_max_f32_e32 v48, 0, v48
	v_max_f32_e32 v49, 0, v49
	v_pk_add_f32 v[38:39], v[38:39], v[46:47]
	v_pk_add_f32 v[36:37], v[36:37], v[48:49]
	v_add_u32_e32 v46, 9, v44
	v_cmp_lt_i32_e64 s[14:15], v46, v45
	s_mov_b64 exec, s[14:15]
	global_load_dwordx4 v[64:67], v29, s[12:13] offset:2304
	s_waitcnt lgkmcnt(0)
	v_lshl_add_u32 v62, v62, 8, v26
	global_load_dwordx4 v[68:71], v62, s[4:5]
	ds_read_b32 v62, v27 offset:56
	s_mov_b64 exec, s[22:23]
	v_add_u32_e32 v44, 5, v44
	v_add_u32_e32 v27, 20, v27
	v_add_u32_e32 v29, 0x500, v29
	s_cmp_lg_u64 s[2:3], 0
	s_cbranch_scc1 .Ll5_p1_loop
	s_branch .Ll5_p1_done

.Ll5_p1_done:
	s_movk_i32 s2, 0x110
	v_cvt_pk_f16_f32 v5, v36, v37
	v_cvt_pk_f16_f32 v4, v38, v39
	v_cvt_pk_f16_f32 v3, v40, v41
	v_cvt_pk_f16_f32 v2, v42, v43
	v_and_b32_e32 v46, 30, v35
	v_mad_u32_u24 v46, v46, s2, v26
	ds_write_b128 v46, v[2:5]
	v_or_b32_e32 v47, 1, v35
	v_mov_b32_e32 v46, 0x3200
	v_lshl_or_b32 v46, v47, 2, v46
	ds_read2_b32 v[44:45], v46 offset1:1
	v_add_u32_e32 v46, s24, v47
	s_mov_b32 s2, 0x186a0
	v_cmp_gt_i32_e32 vcc, s2, v46
	v_cvt_f32_f16_e32 v42, v30
	v_cvt_f32_f16_sdwa v43, v30 dst_sel:DWORD dst_unused:UNUSED_PAD src0_sel:WORD_1
	v_cvt_f32_f16_e32 v40, v31
	v_cvt_f32_f16_sdwa v41, v31 dst_sel:DWORD dst_unused:UNUSED_PAD src0_sel:WORD_1
	v_cvt_f32_f16_e32 v38, v32
	v_cvt_f32_f16_sdwa v39, v32 dst_sel:DWORD dst_unused:UNUSED_PAD src0_sel:WORD_1
	v_cvt_f32_f16_e32 v36, v33
	v_cvt_f32_f16_sdwa v37, v33 dst_sel:DWORD dst_unused:UNUSED_PAD src0_sel:WORD_1
	v_mul_f32_e32 v36, v34, v36
	v_mul_f32_e32 v37, v34, v37
	v_mul_f32_e32 v38, v34, v38
	v_mul_f32_e32 v39, v34, v39
	v_mul_f32_e32 v40, v34, v40
	v_mul_f32_e32 v41, v34, v41
	v_mul_f32_e32 v42, v34, v42
	v_mul_f32_e32 v43, v34, v43
	v_cndmask_b32_e32 v36, 0, v36, vcc
	v_cndmask_b32_e32 v37, 0, v37, vcc
	v_cndmask_b32_e32 v38, 0, v38, vcc
	v_cndmask_b32_e32 v39, 0, v39, vcc
	v_cndmask_b32_e32 v40, 0, v40, vcc
	v_cndmask_b32_e32 v41, 0, v41, vcc
	v_cndmask_b32_e32 v42, 0, v42, vcc
	v_cndmask_b32_e32 v43, 0, v43, vcc
	s_waitcnt lgkmcnt(0)
	v_sub_u32_e32 v27, v44, v28
	v_lshl_add_u32 v27, v27, 2, s0
	v_lshl_add_u32 v29, v44, 8, v26
	v_cmp_lt_i32_e64 s[2:3], v44, v45
	v_add_u32_e32 v46, 1, v44
	v_cmp_lt_i32_e64 s[16:17], v46, v45
	v_add_u32_e32 v46, 2, v44
	v_cmp_lt_i32_e64 s[18:19], v46, v45
	v_add_u32_e32 v46, 3, v44
	v_cmp_lt_i32_e64 s[20:21], v46, v45
	v_add_u32_e32 v46, 4, v44
	v_cmp_lt_i32_e64 s[14:15], v46, v45
	s_mov_b64 exec, s[2:3]
	ds_read_b32 v2, v27 offset:0
	global_load_dwordx4 v[4:7], v29, s[12:13] offset:0
	s_waitcnt lgkmcnt(0)
	v_lshl_add_u32 v2, v2, 8, v26
	global_load_dwordx4 v[8:11], v2, s[4:5]
	ds_read_b32 v2, v27 offset:20
	s_mov_b64 exec, s[16:17]
	ds_read_b32 v3, v27 offset:4
	global_load_dwordx4 v[12:15], v29, s[12:13] offset:256
	s_waitcnt lgkmcnt(0)
	v_lshl_add_u32 v3, v3, 8, v26
	global_load_dwordx4 v[16:19], v3, s[4:5]
	ds_read_b32 v3, v27 offset:24
	s_mov_b64 exec, s[18:19]
	ds_read_b32 v24, v27 offset:8
	global_load_dwordx4 v[20:23], v29, s[12:13] offset:512
	s_waitcnt lgkmcnt(0)
	v_lshl_add_u32 v24, v24, 8, v26
	global_load_dwordx4 v[50:53], v24, s[4:5]
	ds_read_b32 v24, v27 offset:28
	s_mov_b64 exec, s[20:21]
	ds_read_b32 v25, v27 offset:12
	global_load_dwordx4 v[54:57], v29, s[12:13] offset:768
	s_waitcnt lgkmcnt(0)
	v_lshl_add_u32 v25, v25, 8, v26
	global_load_dwordx4 v[58:61], v25, s[4:5]
	ds_read_b32 v25, v27 offset:32
	s_mov_b64 exec, s[14:15]
	ds_read_b32 v62, v27 offset:16
	global_load_dwordx4 v[64:67], v29, s[12:13] offset:1024
	s_waitcnt lgkmcnt(0)
	v_lshl_add_u32 v62, v62, 8, v26
	global_load_dwordx4 v[68:71], v62, s[4:5]
	ds_read_b32 v62, v27 offset:36
	s_mov_b64 exec, s[22:23]
	s_cmp_eq_u64 s[2:3], 0
	s_cbranch_scc1 .Ll5_p2_empty

	.amdhsa_kernel _Z12layer_kernelILb0ELi256ELi32EEvPKDv8_DF16_PKfPS0_PiS6_S6_S2_S4_S5_PfPK15HIP_vector_typeIiLj2EEPKi
		.amdhsa_group_segment_fixed_size 22000
		.amdhsa_private_segment_fixed_size 0
		.amdhsa_kernarg_size 352
		.amdhsa_user_sgpr_count 2
		.amdhsa_user_sgpr_dispatch_ptr 0
		.amdhsa_user_sgpr_queue_ptr 0
		.amdhsa_user_sgpr_kernarg_segment_ptr 1
		.amdhsa_user_sgpr_dispatch_id 0
		.amdhsa_user_sgpr_kernarg_preload_length 0
		.amdhsa_user_sgpr_kernarg_preload_offset 0
		.amdhsa_user_sgpr_private_segment_size 0
		.amdhsa_uses_dynamic_stack 0
		.amdhsa_enable_private_segment 0
		.amdhsa_system_sgpr_workgroup_id_x 1
		.amdhsa_system_sgpr_workgroup_id_y 0
		.amdhsa_system_sgpr_workgroup_id_z 0
		.amdhsa_system_sgpr_workgroup_info 0
		.amdhsa_system_vgpr_workitem_id 0
		.amdhsa_next_free_vgpr 72
		.amdhsa_next_free_sgpr 30
		.amdhsa_accum_offset 72
		.amdhsa_reserve_vcc 1
		.amdhsa_float_round_mode_32 0
		.amdhsa_float_round_mode_16_64 0
		.amdhsa_float_denorm_mode_32 3
		.amdhsa_float_denorm_mode_16_64 3
		.amdhsa_dx10_clamp 1
		.amdhsa_ieee_mode 1
		.amdhsa_fp16_overflow 0
		.amdhsa_tg_split 0
		.amdhsa_exception_fp_ieee_invalid_op 0
		.amdhsa_exception_fp_denorm_src 0
		.amdhsa_exception_fp_ieee_div_zero 0
		.amdhsa_exception_fp_ieee_overflow 0
		.amdhsa_exception_fp_ieee_underflow 0
		.amdhsa_exception_fp_ieee_inexact 0
		.amdhsa_exception_int_div_zero 0
	.end_amdhsa_kernel

amdhsa.kernels:
  - .agpr_count:     0
    .args:
      - .actual_access:  read_only
        .address_space:  global
        .offset:         0
        .size:           8
        .value_kind:     global_buffer
      - .address_space:  global
        .offset:         8
        .size:           8
        .value_kind:     global_buffer
      - .actual_access:  read_only
        .address_space:  global
        .offset:         16
        .size:           8
        .value_kind:     global_buffer
      - .actual_access:  read_only
        .address_space:  global
        .offset:         24
        .size:           8
        .value_kind:     global_buffer
      - .actual_access:  write_only
        .address_space:  global
        .offset:         32
        .size:           8
        .value_kind:     global_buffer
      - .actual_access:  read_only
        .address_space:  global
        .offset:         40
        .size:           8
        .value_kind:     global_buffer
      - .actual_access:  write_only
        .address_space:  global
        .offset:         48
        .size:           8
        .value_kind:     global_buffer
      - .actual_access:  write_only
        .address_space:  global
        .offset:         56
        .size:           8
        .value_kind:     global_buffer
    .group_segment_fixed_size: 6400
    .kernarg_segment_align: 8
    .kernarg_segment_size: 64
    .language:       OpenCL C
    .language_version:
      - 2
      - 0
    .max_flat_workgroup_size: 1024
    .name:           _Z17prep_count_kernelPKfPDv8_DF16_S0_S0_S2_PKiPiP15HIP_vector_typeIfLj4EE
    .private_segment_fixed_size: 0
    .sgpr_count:     22
    .sgpr_spill_count: 0
    .symbol:         _Z17prep_count_kernelPKfPDv8_DF16_S0_S0_S2_PKiPiP15HIP_vector_typeIfLj4EE.kd
    .uniform_work_group_size: 1
    .uses_dynamic_stack: false
    .vgpr_count:     22
    .vgpr_spill_count: 0
    .wavefront_size: 64
  - .agpr_count:     0
    .args:
      - .actual_access:  read_only
        .address_space:  global
        .offset:         0
        .size:           8
        .value_kind:     global_buffer
      - .actual_access:  read_only
        .address_space:  global
        .offset:         8
        .size:           8
        .value_kind:     global_buffer
      - .actual_access:  read_only
        .address_space:  global
        .offset:         16
        .size:           8
        .value_kind:     global_buffer
      - .actual_access:  write_only
        .address_space:  global
        .offset:         24
        .size:           8
        .value_kind:     global_buffer
      - .actual_access:  write_only
        .address_space:  global
        .offset:         32
        .size:           8
        .value_kind:     global_buffer
    .group_segment_fixed_size: 124704
    .kernarg_segment_align: 8
    .kernarg_segment_size: 40
    .language:       OpenCL C
    .language_version:
      - 2
      - 0
    .max_flat_workgroup_size: 1024
    .name:           _Z14scatter_kernelPKiS0_S0_PiP15HIP_vector_typeIiLj2EE
    .private_segment_fixed_size: 0
    .sgpr_count:     55
    .sgpr_spill_count: 0
    .symbol:         _Z14scatter_kernelPKiS0_S0_PiP15HIP_vector_typeIiLj2EE.kd
    .uniform_work_group_size: 1
    .uses_dynamic_stack: false
    .vgpr_count:     128
    .vgpr_spill_count: 0
    .wavefront_size: 64
  - .agpr_count:     0
    .args:
      - .actual_access:  read_only
        .address_space:  global
        .offset:         0
        .size:           8
        .value_kind:     global_buffer
      - .address_space:  global
        .offset:         8
        .size:           8
        .value_kind:     global_buffer
      - .address_space:  global
        .offset:         16
        .size:           8
        .value_kind:     global_buffer
      - .actual_access:  read_only
        .address_space:  global
        .offset:         24
        .size:           8
        .value_kind:     global_buffer
      - .actual_access:  read_only
        .address_space:  global
        .offset:         32
        .size:           8
        .value_kind:     global_buffer
      - .actual_access:  read_only
        .address_space:  global
        .offset:         40
        .size:           8
        .value_kind:     global_buffer
      - .offset:         48
        .size:           4
        .value_kind:     hidden_block_count_x
      - .offset:         52
        .size:           4
        .value_kind:     hidden_block_count_y
      - .offset:         56
        .size:           4
        .value_kind:     hidden_block_count_z
      - .offset:         60
        .size:           2
        .value_kind:     hidden_group_size_x
      - .offset:         62
        .size:           2
        .value_kind:     hidden_group_size_y
      - .offset:         64
        .size:           2
        .value_kind:     hidden_group_size_z
      - .offset:         66
        .size:           2
        .value_kind:     hidden_remainder_x
      - .offset:         68
        .size:           2
        .value_kind:     hidden_remainder_y
      - .offset:         70
        .size:           2
        .value_kind:     hidden_remainder_z
      - .offset:         88
        .size:           8
        .value_kind:     hidden_global_offset_x
      - .offset:         96
        .size:           8
        .value_kind:     hidden_global_offset_y
      - .offset:         104
        .size:           8
        .value_kind:     hidden_global_offset_z
      - .offset:         112
        .size:           2
        .value_kind:     hidden_grid_dims
    .group_segment_fixed_size: 1024
    .kernarg_segment_align: 8
    .kernarg_segment_size: 304
    .language:       OpenCL C
    .language_version:
      - 2
      - 0
    .max_flat_workgroup_size: 256
    .name:           _Z9bn_kernelPKDv8_DF16_S1_PS_PKfS4_S4_
    .private_segment_fixed_size: 0
    .sgpr_count:     20
    .sgpr_spill_count: 0
    .symbol:         _Z9bn_kernelPKDv8_DF16_S1_PS_PKfS4_S4_.kd
    .uniform_work_group_size: 1
    .uses_dynamic_stack: false
    .vgpr_count:     64
    .vgpr_spill_count: 0
    .wavefront_size: 64
  - .agpr_count:     0
    .args:
      - .actual_access:  read_only
        .address_space:  global
        .offset:         0
        .size:           8
        .value_kind:     global_buffer
      - .actual_access:  read_only
        .address_space:  global
        .offset:         8
        .size:           8
        .value_kind:     global_buffer
      - .actual_access:  read_only
        .address_space:  global
        .offset:         16
        .size:           8
        .value_kind:     global_buffer
      - .actual_access:  read_only
        .address_space:  global
        .offset:         24
        .size:           8
        .value_kind:     global_buffer
      - .actual_access:  read_only
        .address_space:  global
        .offset:         32
        .size:           8
        .value_kind:     global_buffer
      - .actual_access:  read_only
        .address_space:  global
        .offset:         40
        .size:           8
        .value_kind:     global_buffer
      - .actual_access:  read_only
        .address_space:  global
        .offset:         48
        .size:           8
        .value_kind:     global_buffer
      - .actual_access:  write_only
        .address_space:  global
        .offset:         56
        .size:           8
        .value_kind:     global_buffer
      - .offset:         64
        .size:           4
        .value_kind:     hidden_block_count_x
      - .offset:         68
        .size:           4
        .value_kind:     hidden_block_count_y
      - .offset:         72
        .size:           4
        .value_kind:     hidden_block_count_z
      - .offset:         76
        .size:           2
        .value_kind:     hidden_group_size_x
      - .offset:         78
        .size:           2
        .value_kind:     hidden_group_size_y
      - .offset:         80
        .size:           2
        .value_kind:     hidden_group_size_z
      - .offset:         82
        .size:           2
        .value_kind:     hidden_remainder_x
      - .offset:         84
        .size:           2
        .value_kind:     hidden_remainder_y
      - .offset:         86
        .size:           2
        .value_kind:     hidden_remainder_z
      - .offset:         104
        .size:           8
        .value_kind:     hidden_global_offset_x
      - .offset:         112
        .size:           8
        .value_kind:     hidden_global_offset_y
      - .offset:         120
        .size:           8
        .value_kind:     hidden_global_offset_z
      - .offset:         128
        .size:           2
        .value_kind:     hidden_grid_dims
    .group_segment_fixed_size: 34816
    .kernarg_segment_align: 8
    .kernarg_segment_size: 320
    .language:       OpenCL C
    .language_version:
      - 2
      - 0
    .max_flat_workgroup_size: 512
    .name:           _Z12final_kernelPKDv8_DF16_S1_PKfS3_S3_S1_S3_Pf
    .private_segment_fixed_size: 0
    .sgpr_count:     34
    .sgpr_spill_count: 0
    .symbol:         _Z12final_kernelPKDv8_DF16_S1_PKfS3_S3_S1_S3_Pf.kd
    .uniform_work_group_size: 1
    .uses_dynamic_stack: false
    .vgpr_count:     60
    .vgpr_spill_count: 0
    .wavefront_size: 64
  - .agpr_count:     0
    .args:
      - .actual_access:  read_only
        .address_space:  global
        .offset:         0
        .size:           8
        .value_kind:     global_buffer
      - .actual_access:  read_only
        .address_space:  global
        .offset:         8
        .size:           8
        .value_kind:     global_buffer
      - .address_space:  global
        .offset:         16
        .size:           8
        .value_kind:     global_buffer
      - .actual_access:  write_only
        .address_space:  global
        .offset:         24
        .size:           8
        .value_kind:     global_buffer
      - .address_space:  global
        .offset:         32
        .size:           8
        .value_kind:     global_buffer
      - .address_space:  global
        .offset:         40
        .size:           8
        .value_kind:     global_buffer
      - .actual_access:  read_only
        .address_space:  global
        .offset:         48
        .size:           8
        .value_kind:     global_buffer
      - .actual_access:  read_only
        .address_space:  global
        .offset:         56
        .size:           8
        .value_kind:     global_buffer
      - .address_space:  global
        .offset:         64
        .size:           8
        .value_kind:     global_buffer
      - .address_space:  global
        .offset:         72
        .size:           8
        .value_kind:     global_buffer
      - .actual_access:  read_only
        .address_space:  global
        .offset:         80
        .size:           8
        .value_kind:     global_buffer
      - .actual_access:  read_only
        .address_space:  global
        .offset:         88
        .size:           8
        .value_kind:     global_buffer
      - .offset:         96
        .size:           4
        .value_kind:     hidden_block_count_x
      - .offset:         100
        .size:           4
        .value_kind:     hidden_block_count_y
      - .offset:         104
        .size:           4
        .value_kind:     hidden_block_count_z
      - .offset:         108
        .size:           2
        .value_kind:     hidden_group_size_x
      - .offset:         110
        .size:           2
        .value_kind:     hidden_group_size_y
      - .offset:         112
        .size:           2
        .value_kind:     hidden_group_size_z
      - .offset:         114
        .size:           2
        .value_kind:     hidden_remainder_x
      - .offset:         116
        .size:           2
        .value_kind:     hidden_remainder_y
      - .offset:         118
        .size:           2
        .value_kind:     hidden_remainder_z
      - .offset:         136
        .size:           8
        .value_kind:     hidden_global_offset_x
      - .offset:         144
        .size:           8
        .value_kind:     hidden_global_offset_y
      - .offset:         152
        .size:           8
        .value_kind:     hidden_global_offset_z
      - .offset:         160
        .size:           2
        .value_kind:     hidden_grid_dims
    .group_segment_fixed_size: 26384
    .kernarg_segment_align: 8
    .kernarg_segment_size: 352
    .language:       OpenCL C
    .language_version:
      - 2
      - 0
    .max_flat_workgroup_size: 512
    .name:           _Z12layer_kernelILb1ELi512ELi64EEvPKDv8_DF16_PKfPS0_PiS6_S6_S2_S4_S5_PfPK15HIP_vector_typeIiLj2EEPKi
    .private_segment_fixed_size: 0
    .sgpr_count:     52
    .sgpr_spill_count: 0
    .symbol:         _Z12layer_kernelILb1ELi512ELi64EEvPKDv8_DF16_PKfPS0_PiS6_S6_S2_S4_S5_PfPK15HIP_vector_typeIiLj2EEPKi.kd
    .uniform_work_group_size: 1
    .uses_dynamic_stack: false
    .vgpr_count:     61
    .vgpr_spill_count: 0
    .wavefront_size: 64
  - .agpr_count:     0
    .args:
      - .actual_access:  read_only
        .address_space:  global
        .offset:         0
        .size:           8
        .value_kind:     global_buffer
      - .actual_access:  read_only
        .address_space:  global
        .offset:         8
        .size:           8
        .value_kind:     global_buffer
      - .actual_access:  read_only
        .address_space:  global
        .offset:         16
        .size:           8
        .value_kind:     global_buffer
      - .actual_access:  read_only
        .address_space:  global
        .offset:         24
        .size:           8
        .value_kind:     global_buffer
      - .actual_access:  read_only
        .address_space:  global
        .offset:         32
        .size:           8
        .value_kind:     global_buffer
      - .actual_access:  read_only
        .address_space:  global
        .offset:         40
        .size:           8
        .value_kind:     global_buffer
      - .actual_access:  read_only
        .address_space:  global
        .offset:         48
        .size:           8
        .value_kind:     global_buffer
      - .actual_access:  read_only
        .address_space:  global
        .offset:         56
        .size:           8
        .value_kind:     global_buffer
      - .address_space:  global
        .offset:         64
        .size:           8
        .value_kind:     global_buffer
      - .address_space:  global
        .offset:         72
        .size:           8
        .value_kind:     global_buffer
      - .actual_access:  read_only
        .address_space:  global
        .offset:         80
        .size:           8
        .value_kind:     global_buffer
      - .actual_access:  read_only
        .address_space:  global
        .offset:         88
        .size:           8
        .value_kind:     global_buffer
      - .offset:         96
        .size:           4
        .value_kind:     hidden_block_count_x
      - .offset:         100
        .size:           4
        .value_kind:     hidden_block_count_y
      - .offset:         104
        .size:           4
        .value_kind:     hidden_block_count_z
      - .offset:         108
        .size:           2
        .value_kind:     hidden_group_size_x
      - .offset:         110
        .size:           2
        .value_kind:     hidden_group_size_y
      - .offset:         112
        .size:           2
        .value_kind:     hidden_group_size_z
      - .offset:         114
        .size:           2
        .value_kind:     hidden_remainder_x
      - .offset:         116
        .size:           2
        .value_kind:     hidden_remainder_y
      - .offset:         118
        .size:           2
        .value_kind:     hidden_remainder_z
      - .offset:         136
        .size:           8
        .value_kind:     hidden_global_offset_x
      - .offset:         144
        .size:           8
        .value_kind:     hidden_global_offset_y
      - .offset:         152
        .size:           8
        .value_kind:     hidden_global_offset_z
      - .offset:         160
        .size:           2
        .value_kind:     hidden_grid_dims
    .group_segment_fixed_size: 22000
    .kernarg_segment_align: 8
    .kernarg_segment_size: 352
    .language:       OpenCL C
    .language_version:
      - 2
      - 0
    .max_flat_workgroup_size: 256
    .name:           _Z12layer_kernelILb0ELi256ELi32EEvPKDv8_DF16_PKfPS0_PiS6_S6_S2_S4_S5_PfPK15HIP_vector_typeIiLj2EEPKi
    .private_segment_fixed_size: 0
    .sgpr_count:     36
    .sgpr_spill_count: 0
    .symbol:         _Z12layer_kernelILb0ELi256ELi32EEvPKDv8_DF16_PKfPS0_PiS6_S6_S2_S4_S5_PfPK15HIP_vector_typeIiLj2EEPKi.kd
    .uniform_work_group_size: 1
    .uses_dynamic_stack: false
    .vgpr_count:     72
    .vgpr_spill_count: 0
    .wavefront_size: 64
